# LSTM step barrier: sleepless poll at priority 0
# baseline (speedup 1.0000x reference)
.Lb1_poll:
	ds_read_b32 v52, v56
	s_waitcnt lgkmcnt(0)
	v_readfirstlane_b32 s6, v52
	s_cmp_ge_i32 s6, s10
	s_cbranch_scc1 .LBB1_370
	s_branch .Lb1_poll

.Lb0_poll:
	ds_read_b32 v70, v75
	s_waitcnt lgkmcnt(0)
	v_readfirstlane_b32 s10, v70
	s_cmp_ge_i32 s10, s9
	s_cbranch_scc1 .LBB1_424
	s_branch .Lb0_poll
